# MoE K loop: waves 4-7 issue their step loads after the MFMAs, waves 0-3 before (SIMD partners no longer stall on VMEM issue together)
# baseline (speedup 1.0000x reference)
.LBB0_3308:
	s_or_b64 exec, exec, s[0:1]
	s_waitcnt lgkmcnt(0)
	s_barrier
	v_readfirstlane_b32 s56, v0
	s_nop 1
	s_bfe_u32 s55, s56, 0x10008

.LBB0_3326:
	s_add_i32 s15, s16, 2
	s_add_i32 s16, s16, 4
	s_min_u32 s16, s16, 63
	s_mul_i32 s17, s14, 0xa000
	s_lshl_b32 s64, s16, 6
	s_add_i32 s20, s17, 0xffff6000
	s_cmp_lg_u32 s14, 0
	s_cselect_b32 s20, s20, 0x14000
	s_add_i32 s20, s18, s20
	s_waitcnt lgkmcnt(0)
	s_barrier
	s_cmp_lt_u32 s15, 62
	s_cbranch_scc0 .Lskipv_51971
	s_cmp_eq_u32 s55, 0
	s_cbranch_scc0 .Lstg_a51971
	v_lshl_add_u64 v[156:157], v[202:203], 0, s[64:65]
	s_mov_b32 m0, s20
	s_nop 0
	global_load_lds_dwordx4 v[156:157], off
	v_lshl_add_u64 v[156:157], v[204:205], 0, s[64:65]
	s_add_i32 m0, s20, 0x400
	s_nop 0
	global_load_lds_dwordx4 v[156:157], off
	v_lshl_add_u64 v[156:157], v[206:207], 0, s[64:65]
	s_add_i32 m0, s20, 0x800
	s_nop 0
	global_load_lds_dwordx4 v[156:157], off
	v_lshl_add_u64 v[156:157], v[208:209], 0, s[64:65]
	s_add_i32 m0, s20, 0xc00
	s_nop 0
	global_load_lds_dwordx4 v[156:157], off
	v_lshl_add_u64 v[156:157], v[210:211], 0, s[64:65]
	s_add_i32 m0, s20, 0x1000
	s_lshl_b32 s64, s16, 16
	global_load_lds_dwordx4 v[156:157], off
	v_lshl_add_u64 v[160:161], v[212:213], 0, s[64:65]
	global_load_dwordx4 v[156:159], v[160:161], off nt
	s_nop 0
	global_load_dwordx4 v[160:163], v[160:161], off offset:2048 nt
.Lstg_a51971:
.Lskipv_51971:
	v_add_u32_e32 v167, s17, v86
	ds_read2_b32 v[168:169], v201 offset0:0 offset1:0x84
	ds_read2_b32 v[170:171], v232 offset0:0 offset1:0x84
	ds_read2_b32 v[172:173], v201 offset0:16 offset1:0x94
	ds_read2_b32 v[174:175], v232 offset0:16 offset1:0x94
	ds_read2_b32 v[176:177], v201 offset0:32 offset1:0xa4
	ds_read2_b32 v[178:179], v232 offset0:32 offset1:0xa4
	ds_read2_b32 v[180:181], v201 offset0:48 offset1:0xb4
	ds_read2_b32 v[182:183], v232 offset0:48 offset1:0xb4
	ds_read_b128 v[184:187], v167 offset:0
	ds_read_b128 v[188:191], v167 offset:0x400
	s_nop 0
	s_waitcnt lgkmcnt(1)
	s_setprio 1
	v_mfma_f32_16x16x32_bf16 v[140:143], v[168:171], v[184:187], v[140:143]
	v_mfma_f32_16x16x32_bf16 v[132:135], v[172:175], v[184:187], v[132:135]
	v_mfma_f32_16x16x32_bf16 v[144:147], v[176:179], v[184:187], v[144:147]
	v_mfma_f32_16x16x32_bf16 v[136:139], v[180:183], v[184:187], v[136:139]
	ds_read_b128 v[184:187], v167 offset:0x800
	s_waitcnt lgkmcnt(1)
	s_nop 0
	v_mfma_f32_16x16x32_bf16 v[124:127], v[168:171], v[188:191], v[124:127]
	v_mfma_f32_16x16x32_bf16 v[112:115], v[172:175], v[188:191], v[112:115]
	v_mfma_f32_16x16x32_bf16 v[128:131], v[176:179], v[188:191], v[128:131]
	v_mfma_f32_16x16x32_bf16 v[116:119], v[180:183], v[188:191], v[116:119]
	ds_read_b128 v[188:191], v167 offset:0xc00
	s_waitcnt lgkmcnt(1)
	s_nop 0
	v_mfma_f32_16x16x32_bf16 v[82:85], v[168:171], v[184:187], v[82:85]
	v_mfma_f32_16x16x32_bf16 v[54:57], v[172:175], v[184:187], v[54:57]
	v_mfma_f32_16x16x32_bf16 v[88:91], v[176:179], v[184:187], v[88:91]
	v_mfma_f32_16x16x32_bf16 v[58:61], v[180:183], v[184:187], v[58:61]
	ds_read_b128 v[184:187], v167 offset:0x1000
	s_waitcnt lgkmcnt(1)
	s_nop 0
	v_mfma_f32_16x16x32_bf16 v[26:29], v[168:171], v[188:191], v[26:29]
	v_mfma_f32_16x16x32_bf16 v[6:9], v[172:175], v[188:191], v[6:9]
	v_mfma_f32_16x16x32_bf16 v[42:45], v[176:179], v[188:191], v[42:45]
	v_mfma_f32_16x16x32_bf16 v[14:17], v[180:183], v[188:191], v[14:17]
	ds_read_b128 v[188:191], v167 offset:0x1400
	s_waitcnt lgkmcnt(1)
	s_nop 0
	v_mfma_f32_16x16x32_bf16 v[92:95], v[168:171], v[184:187], v[92:95]
	v_mfma_f32_16x16x32_bf16 v[62:65], v[172:175], v[184:187], v[62:65]
	v_mfma_f32_16x16x32_bf16 v[96:99], v[176:179], v[184:187], v[96:99]
	v_mfma_f32_16x16x32_bf16 v[66:69], v[180:183], v[184:187], v[66:69]
	ds_read_b128 v[184:187], v167 offset:0x1800
	s_waitcnt lgkmcnt(1)
	s_nop 0
	v_mfma_f32_16x16x32_bf16 v[38:41], v[168:171], v[188:191], v[38:41]
	v_mfma_f32_16x16x32_bf16 v[18:21], v[172:175], v[188:191], v[18:21]
	v_mfma_f32_16x16x32_bf16 v[46:49], v[176:179], v[188:191], v[46:49]
	v_mfma_f32_16x16x32_bf16 v[22:25], v[180:183], v[188:191], v[22:25]
	ds_read_b128 v[188:191], v167 offset:0x1c00
	s_waitcnt lgkmcnt(1)
	s_nop 0
	v_mfma_f32_16x16x32_bf16 v[108:111], v[168:171], v[184:187], v[108:111]
	s_waitcnt lgkmcnt(0)
	v_mfma_f32_16x16x32_bf16 v[100:103], v[172:175], v[184:187], v[100:103]
	v_mfma_f32_16x16x32_bf16 v[120:123], v[176:179], v[184:187], v[120:123]
	v_mfma_f32_16x16x32_bf16 v[104:107], v[180:183], v[184:187], v[104:107]
	v_mfma_f32_16x16x32_bf16 v[70:73], v[168:171], v[188:191], v[70:73]
	v_mfma_f32_16x16x32_bf16 v[50:53], v[172:175], v[188:191], v[50:53]
	v_mfma_f32_16x16x32_bf16 v[10:13], v[176:179], v[188:191], v[10:13]
	v_mfma_f32_16x16x32_bf16 v[2:5], v[180:183], v[188:191], v[2:5]
	s_cmp_lt_u32 s15, 62
	s_cbranch_scc0 .Lstg_b51971
	s_cmp_eq_u32 s55, 0
	s_cbranch_scc1 .Lstg_b51971
	v_lshl_add_u64 v[156:157], v[202:203], 0, s[64:65]
	s_mov_b32 m0, s20
	s_nop 0
	global_load_lds_dwordx4 v[156:157], off
	v_lshl_add_u64 v[156:157], v[204:205], 0, s[64:65]
	s_add_i32 m0, s20, 0x400
	s_nop 0
	global_load_lds_dwordx4 v[156:157], off
	v_lshl_add_u64 v[156:157], v[206:207], 0, s[64:65]
	s_add_i32 m0, s20, 0x800
	s_nop 0
	global_load_lds_dwordx4 v[156:157], off
	v_lshl_add_u64 v[156:157], v[208:209], 0, s[64:65]
	s_add_i32 m0, s20, 0xc00
	s_nop 0
	global_load_lds_dwordx4 v[156:157], off
	v_lshl_add_u64 v[156:157], v[210:211], 0, s[64:65]
	s_add_i32 m0, s20, 0x1000
	s_lshl_b32 s64, s16, 16
	global_load_lds_dwordx4 v[156:157], off
	v_lshl_add_u64 v[160:161], v[212:213], 0, s[64:65]
	global_load_dwordx4 v[156:159], v[160:161], off nt
	s_nop 0
	global_load_dwordx4 v[160:163], v[160:161], off offset:2048 nt
.Lstg_b51971:
	s_setprio 0
	s_cmp_lt_u32 s15, 62
	s_cbranch_scc1 .Lokw_51971
	s_waitcnt vmcnt(0)
.Lokw_51971:
	s_add_i32 s16, s14, 1
	s_cmp_lg_u32 s14, 2
	s_cselect_b32 s14, s16, 0
	s_min_u32 s16, s15, 60
	s_add_i32 s16, s16, 3
	s_mul_i32 s17, s14, 0xa000
	s_lshl_b32 s64, s16, 6
	s_add_i32 s20, s17, 0xffff6000
	s_cmp_lg_u32 s14, 0
	s_waitcnt vmcnt(7)
	v_cvt_pk_bf16_f32 v148, v152, v148
	v_add_u32_e32 v152, 0x20100, v165
	s_cselect_b32 s20, s20, 0x14000
	v_cvt_pk_bf16_f32 v149, v153, v149
	v_cvt_pk_bf16_f32 v150, v154, v150
	v_cvt_pk_bf16_f32 v151, v155, v151
	ds_write_b128 v152, v[148:151]
	v_lshl_add_u64 v[168:169], v[202:203], 0, s[64:65]
	v_lshl_add_u64 v[170:171], v[204:205], 0, s[64:65]
	v_lshl_add_u64 v[172:173], v[206:207], 0, s[64:65]
	v_lshl_add_u64 v[174:175], v[208:209], 0, s[64:65]
	v_lshl_add_u64 v[176:177], v[210:211], 0, s[64:65]
	s_lshl_b32 s64, s16, 16
	s_add_i32 s16, s18, s20
	s_waitcnt lgkmcnt(0)
	s_barrier
	s_cmp_lt_u32 s15, 62
	s_cbranch_scc0 .Lskipv_52148
	s_cmp_eq_u32 s55, 0
	s_cbranch_scc0 .Lstg_a52148
	v_lshl_add_u64 v[148:149], v[212:213], 0, s[64:65]
	s_mov_b32 m0, s16
	global_load_dwordx4 v[152:155], v[148:149], off nt
	s_nop 0
	global_load_dwordx4 v[148:151], v[148:149], off offset:2048 nt
	s_nop 0
	global_load_lds_dwordx4 v[168:169], off
	s_add_i32 m0, s16, 0x400
	s_nop 0
	global_load_lds_dwordx4 v[170:171], off
	s_add_i32 m0, s16, 0x800
	s_nop 0
	global_load_lds_dwordx4 v[172:173], off
	s_add_i32 m0, s16, 0xc00
	s_nop 0
	global_load_lds_dwordx4 v[174:175], off
	s_add_i32 m0, s16, 0x1000
	s_nop 0
	global_load_lds_dwordx4 v[176:177], off
.Lstg_a52148:
.Lskipv_52148:
	v_add_u32_e32 v167, s17, v86
	ds_read2_b32 v[168:169], v233 offset0:0 offset1:0x84
	ds_read2_b32 v[170:171], v234 offset0:0 offset1:0x84
	ds_read2_b32 v[172:173], v233 offset0:16 offset1:0x94
	ds_read2_b32 v[174:175], v234 offset0:16 offset1:0x94
	ds_read2_b32 v[176:177], v233 offset0:32 offset1:0xa4
	ds_read2_b32 v[178:179], v234 offset0:32 offset1:0xa4
	ds_read2_b32 v[180:181], v233 offset0:48 offset1:0xb4
	ds_read2_b32 v[182:183], v234 offset0:48 offset1:0xb4
	ds_read_b128 v[184:187], v167 offset:0
	ds_read_b128 v[188:191], v167 offset:0x400
	s_nop 0
	s_waitcnt lgkmcnt(1)
	s_setprio 1
	v_mfma_f32_16x16x32_bf16 v[140:143], v[168:171], v[184:187], v[140:143]
	v_mfma_f32_16x16x32_bf16 v[132:135], v[172:175], v[184:187], v[132:135]
	v_mfma_f32_16x16x32_bf16 v[144:147], v[176:179], v[184:187], v[144:147]
	v_mfma_f32_16x16x32_bf16 v[136:139], v[180:183], v[184:187], v[136:139]
	ds_read_b128 v[184:187], v167 offset:0x800
	s_waitcnt lgkmcnt(1)
	s_nop 0
	v_mfma_f32_16x16x32_bf16 v[124:127], v[168:171], v[188:191], v[124:127]
	v_mfma_f32_16x16x32_bf16 v[112:115], v[172:175], v[188:191], v[112:115]
	v_mfma_f32_16x16x32_bf16 v[128:131], v[176:179], v[188:191], v[128:131]
	v_mfma_f32_16x16x32_bf16 v[116:119], v[180:183], v[188:191], v[116:119]
	ds_read_b128 v[188:191], v167 offset:0xc00
	s_waitcnt lgkmcnt(1)
	s_nop 0
	v_mfma_f32_16x16x32_bf16 v[82:85], v[168:171], v[184:187], v[82:85]
	v_mfma_f32_16x16x32_bf16 v[54:57], v[172:175], v[184:187], v[54:57]
	v_mfma_f32_16x16x32_bf16 v[88:91], v[176:179], v[184:187], v[88:91]
	v_mfma_f32_16x16x32_bf16 v[58:61], v[180:183], v[184:187], v[58:61]
	ds_read_b128 v[184:187], v167 offset:0x1000
	s_waitcnt lgkmcnt(1)
	s_nop 0
	v_mfma_f32_16x16x32_bf16 v[26:29], v[168:171], v[188:191], v[26:29]
	v_mfma_f32_16x16x32_bf16 v[6:9], v[172:175], v[188:191], v[6:9]
	v_mfma_f32_16x16x32_bf16 v[42:45], v[176:179], v[188:191], v[42:45]
	v_mfma_f32_16x16x32_bf16 v[14:17], v[180:183], v[188:191], v[14:17]
	ds_read_b128 v[188:191], v167 offset:0x1400
	s_waitcnt lgkmcnt(1)
	s_nop 0
	v_mfma_f32_16x16x32_bf16 v[92:95], v[168:171], v[184:187], v[92:95]
	v_mfma_f32_16x16x32_bf16 v[62:65], v[172:175], v[184:187], v[62:65]
	v_mfma_f32_16x16x32_bf16 v[96:99], v[176:179], v[184:187], v[96:99]
	v_mfma_f32_16x16x32_bf16 v[66:69], v[180:183], v[184:187], v[66:69]
	ds_read_b128 v[184:187], v167 offset:0x1800
	s_waitcnt lgkmcnt(1)
	s_nop 0
	v_mfma_f32_16x16x32_bf16 v[38:41], v[168:171], v[188:191], v[38:41]
	v_mfma_f32_16x16x32_bf16 v[18:21], v[172:175], v[188:191], v[18:21]
	v_mfma_f32_16x16x32_bf16 v[46:49], v[176:179], v[188:191], v[46:49]
	v_mfma_f32_16x16x32_bf16 v[22:25], v[180:183], v[188:191], v[22:25]
	ds_read_b128 v[188:191], v167 offset:0x1c00
	s_waitcnt lgkmcnt(1)
	s_nop 0
	v_mfma_f32_16x16x32_bf16 v[108:111], v[168:171], v[184:187], v[108:111]
	s_waitcnt lgkmcnt(0)
	v_mfma_f32_16x16x32_bf16 v[100:103], v[172:175], v[184:187], v[100:103]
	v_mfma_f32_16x16x32_bf16 v[120:123], v[176:179], v[184:187], v[120:123]
	v_mfma_f32_16x16x32_bf16 v[104:107], v[180:183], v[184:187], v[104:107]
	v_mfma_f32_16x16x32_bf16 v[70:73], v[168:171], v[188:191], v[70:73]
	v_mfma_f32_16x16x32_bf16 v[50:53], v[172:175], v[188:191], v[50:53]
	v_mfma_f32_16x16x32_bf16 v[10:13], v[176:179], v[188:191], v[10:13]
	v_mfma_f32_16x16x32_bf16 v[2:5], v[180:183], v[188:191], v[2:5]
	s_cmp_lt_u32 s15, 62
	s_cbranch_scc0 .Lstg_b52148
	s_cmp_eq_u32 s55, 0
	s_cbranch_scc1 .Lstg_b52148
	v_lshl_add_u64 v[148:149], v[212:213], 0, s[64:65]
	s_lshr_b32 s64, s64, 10
	v_lshl_add_u64 v[150:151], v[202:203], 0, s[64:65]
	s_mov_b32 m0, s16
	s_nop 0
	global_load_lds_dwordx4 v[150:151], off
	v_lshl_add_u64 v[150:151], v[204:205], 0, s[64:65]
	s_add_i32 m0, s16, 0x400
	s_nop 0
	global_load_lds_dwordx4 v[150:151], off
	v_lshl_add_u64 v[150:151], v[206:207], 0, s[64:65]
	s_add_i32 m0, s16, 0x800
	s_nop 0
	global_load_lds_dwordx4 v[150:151], off
	v_lshl_add_u64 v[150:151], v[208:209], 0, s[64:65]
	s_add_i32 m0, s16, 0xc00
	s_nop 0
	global_load_lds_dwordx4 v[150:151], off
	v_lshl_add_u64 v[150:151], v[210:211], 0, s[64:65]
	s_add_i32 m0, s16, 0x1000
	s_nop 0
	global_load_lds_dwordx4 v[150:151], off
	global_load_dwordx4 v[152:155], v[148:149], off nt
	s_nop 0
	global_load_dwordx4 v[148:151], v[148:149], off offset:2048 nt

.LBB0_3344:
	s_add_i32 s13, s14, 2
	s_add_i32 s14, s14, 4
	s_min_u32 s14, s14, 63
	s_mul_i32 s15, s12, 0xa000
	s_lshl_b32 s64, s14, 6
	s_add_i32 s16, s15, 0xffff6000
	s_cmp_lg_u32 s12, 0
	s_cselect_b32 s16, s16, 0x14000
	s_add_i32 s16, s18, s16
	s_waitcnt lgkmcnt(0)
	s_barrier
	s_cmp_lt_u32 s13, 62
	s_cbranch_scc0 .Lskipv_53495
	s_cmp_eq_u32 s55, 0
	s_cbranch_scc0 .Lstg_a53495
	v_lshl_add_u64 v[188:189], v[202:203], 0, s[64:65]
	s_mov_b32 m0, s16
	s_nop 0
	global_load_lds_dwordx4 v[188:189], off
	v_lshl_add_u64 v[188:189], v[204:205], 0, s[64:65]
	s_add_i32 m0, s16, 0x400
	s_nop 0
	global_load_lds_dwordx4 v[188:189], off
	v_lshl_add_u64 v[188:189], v[206:207], 0, s[64:65]
	s_add_i32 m0, s16, 0x800
	s_nop 0
	global_load_lds_dwordx4 v[188:189], off
	v_lshl_add_u64 v[188:189], v[208:209], 0, s[64:65]
	s_add_i32 m0, s16, 0xc00
	s_nop 0
	global_load_lds_dwordx4 v[188:189], off
	v_lshl_add_u64 v[188:189], v[210:211], 0, s[64:65]
	s_add_i32 m0, s16, 0x1000
	s_lshl_b32 s64, s14, 16
	global_load_lds_dwordx4 v[188:189], off
	v_lshl_add_u64 v[192:193], v[212:213], 0, s[64:65]
	global_load_dwordx4 v[188:191], v[192:193], off nt
	s_nop 0
	global_load_dwordx4 v[192:195], v[192:193], off offset:2048 nt
.Lstg_a53495:
.Lskipv_53495:
	v_add_u32_e32 v216, s15, v86
	ds_read2_b32 v[196:197], v201 offset0:0 offset1:0x84
	ds_read2_b32 v[198:199], v232 offset0:0 offset1:0x84
	ds_read2_b32 v[222:223], v201 offset0:16 offset1:0x94
	ds_read2_b32 v[224:225], v232 offset0:16 offset1:0x94
	ds_read2_b32 v[226:227], v201 offset0:32 offset1:0xa4
	ds_read2_b32 v[228:229], v232 offset0:32 offset1:0xa4
	ds_read2_b32 v[238:239], v201 offset0:48 offset1:0xb4
	ds_read2_b32 v[240:241], v232 offset0:48 offset1:0xb4
	ds_read_b128 v[242:245], v216 offset:0
	ds_read_b128 v[246:249], v216 offset:0x400
	s_nop 0
	s_waitcnt lgkmcnt(1)
	s_setprio 1
	v_mfma_f32_16x16x32_bf16 v[140:143], v[196:199], v[242:245], v[140:143]
	v_mfma_f32_16x16x32_bf16 v[132:135], v[222:225], v[242:245], v[132:135]
	v_mfma_f32_16x16x32_bf16 v[144:147], v[226:229], v[242:245], v[144:147]
	v_mfma_f32_16x16x32_bf16 v[136:139], v[238:241], v[242:245], v[136:139]
	ds_read_b128 v[242:245], v216 offset:0x800
	s_waitcnt lgkmcnt(1)
	s_nop 0
	v_mfma_f32_16x16x32_bf16 v[124:127], v[196:199], v[246:249], v[124:127]
	v_mfma_f32_16x16x32_bf16 v[112:115], v[222:225], v[246:249], v[112:115]
	v_mfma_f32_16x16x32_bf16 v[128:131], v[226:229], v[246:249], v[128:131]
	v_mfma_f32_16x16x32_bf16 v[116:119], v[238:241], v[246:249], v[116:119]
	ds_read_b128 v[246:249], v216 offset:0xc00
	s_waitcnt lgkmcnt(1)
	s_nop 0
	v_mfma_f32_16x16x32_bf16 v[82:85], v[196:199], v[242:245], v[82:85]
	v_mfma_f32_16x16x32_bf16 v[54:57], v[222:225], v[242:245], v[54:57]
	v_mfma_f32_16x16x32_bf16 v[88:91], v[226:229], v[242:245], v[88:91]
	v_mfma_f32_16x16x32_bf16 v[58:61], v[238:241], v[242:245], v[58:61]
	ds_read_b128 v[242:245], v216 offset:0x1000
	s_waitcnt lgkmcnt(1)
	s_nop 0
	v_mfma_f32_16x16x32_bf16 v[26:29], v[196:199], v[246:249], v[26:29]
	v_mfma_f32_16x16x32_bf16 v[6:9], v[222:225], v[246:249], v[6:9]
	v_mfma_f32_16x16x32_bf16 v[42:45], v[226:229], v[246:249], v[42:45]
	v_mfma_f32_16x16x32_bf16 v[14:17], v[238:241], v[246:249], v[14:17]
	ds_read_b128 v[246:249], v216 offset:0x1400
	s_waitcnt lgkmcnt(1)
	s_nop 0
	v_mfma_f32_16x16x32_bf16 v[92:95], v[196:199], v[242:245], v[92:95]
	v_mfma_f32_16x16x32_bf16 v[62:65], v[222:225], v[242:245], v[62:65]
	v_mfma_f32_16x16x32_bf16 v[96:99], v[226:229], v[242:245], v[96:99]
	v_mfma_f32_16x16x32_bf16 v[66:69], v[238:241], v[242:245], v[66:69]
	ds_read_b128 v[242:245], v216 offset:0x1800
	s_waitcnt lgkmcnt(1)
	s_nop 0
	v_mfma_f32_16x16x32_bf16 v[38:41], v[196:199], v[246:249], v[38:41]
	v_mfma_f32_16x16x32_bf16 v[18:21], v[222:225], v[246:249], v[18:21]
	v_mfma_f32_16x16x32_bf16 v[46:49], v[226:229], v[246:249], v[46:49]
	v_mfma_f32_16x16x32_bf16 v[22:25], v[238:241], v[246:249], v[22:25]
	ds_read_b128 v[246:249], v216 offset:0x1c00
	s_waitcnt lgkmcnt(1)
	s_nop 0
	v_mfma_f32_16x16x32_bf16 v[108:111], v[196:199], v[242:245], v[108:111]
	v_mfma_f32_16x16x32_bf16 v[100:103], v[222:225], v[242:245], v[100:103]
	v_mfma_f32_16x16x32_bf16 v[120:123], v[226:229], v[242:245], v[120:123]
	v_mfma_f32_16x16x32_bf16 v[104:107], v[238:241], v[242:245], v[104:107]
	ds_read_b128 v[242:245], v216 offset:0x2000
	s_waitcnt lgkmcnt(1)
	s_nop 0
	v_mfma_f32_16x16x32_bf16 v[70:73], v[196:199], v[246:249], v[70:73]
	v_mfma_f32_16x16x32_bf16 v[50:53], v[222:225], v[246:249], v[50:53]
	v_mfma_f32_16x16x32_bf16 v[10:13], v[226:229], v[246:249], v[10:13]
	v_mfma_f32_16x16x32_bf16 v[2:5], v[238:241], v[246:249], v[2:5]
	ds_read_b128 v[246:249], v216 offset:0x2400
	s_waitcnt lgkmcnt(1)
	s_nop 0
	v_mfma_f32_16x16x32_bf16 v[176:179], v[196:199], v[242:245], v[176:179]
	s_waitcnt lgkmcnt(0)
	v_mfma_f32_16x16x32_bf16 v[168:171], v[222:225], v[242:245], v[168:171]
	v_mfma_f32_16x16x32_bf16 v[172:175], v[226:229], v[242:245], v[172:175]
	v_mfma_f32_16x16x32_bf16 v[164:167], v[238:241], v[242:245], v[164:167]
	v_mfma_f32_16x16x32_bf16 v[160:163], v[196:199], v[246:249], v[160:163]
	v_mfma_f32_16x16x32_bf16 v[152:155], v[222:225], v[246:249], v[152:155]
	v_mfma_f32_16x16x32_bf16 v[156:159], v[226:229], v[246:249], v[156:159]
	v_mfma_f32_16x16x32_bf16 v[148:151], v[238:241], v[246:249], v[148:151]
	s_cmp_lt_u32 s13, 62
	s_cbranch_scc0 .Lstg_b53495
	s_cmp_eq_u32 s55, 0
	s_cbranch_scc1 .Lstg_b53495
	v_lshl_add_u64 v[188:189], v[202:203], 0, s[64:65]
	s_mov_b32 m0, s16
	s_nop 0
	global_load_lds_dwordx4 v[188:189], off
	v_lshl_add_u64 v[188:189], v[204:205], 0, s[64:65]
	s_add_i32 m0, s16, 0x400
	s_nop 0
	global_load_lds_dwordx4 v[188:189], off
	v_lshl_add_u64 v[188:189], v[206:207], 0, s[64:65]
	s_add_i32 m0, s16, 0x800
	s_nop 0
	global_load_lds_dwordx4 v[188:189], off
	v_lshl_add_u64 v[188:189], v[208:209], 0, s[64:65]
	s_add_i32 m0, s16, 0xc00
	s_nop 0
	global_load_lds_dwordx4 v[188:189], off
	v_lshl_add_u64 v[188:189], v[210:211], 0, s[64:65]
	s_add_i32 m0, s16, 0x1000
	s_lshl_b32 s64, s14, 16
	global_load_lds_dwordx4 v[188:189], off
	v_lshl_add_u64 v[192:193], v[212:213], 0, s[64:65]
	global_load_dwordx4 v[188:191], v[192:193], off nt
	s_nop 0
	global_load_dwordx4 v[192:195], v[192:193], off offset:2048 nt
.Lstg_b53495:
	s_setprio 0
	s_cmp_lt_u32 s13, 62
	s_cbranch_scc1 .Lokw_53495
	s_waitcnt vmcnt(0)
.Lokw_53495:
	s_add_i32 s14, s12, 1
	s_cmp_lg_u32 s12, 2
	s_cselect_b32 s12, s14, 0
	s_min_u32 s14, s13, 60
	s_add_i32 s14, s14, 3
	s_mul_i32 s15, s12, 0xa000
	s_lshl_b32 s64, s14, 6
	s_add_i32 s16, s15, 0xffff6000
	s_cmp_lg_u32 s12, 0
	s_waitcnt vmcnt(7)
	v_cvt_pk_bf16_f32 v180, v184, v180
	v_add_u32_e32 v184, 0x20100, v235
	s_cselect_b32 s16, s16, 0x14000
	v_cvt_pk_bf16_f32 v181, v185, v181
	v_cvt_pk_bf16_f32 v182, v186, v182
	v_cvt_pk_bf16_f32 v183, v187, v183
	ds_write_b128 v184, v[180:183]
	v_lshl_add_u64 v[196:197], v[202:203], 0, s[64:65]
	v_lshl_add_u64 v[198:199], v[204:205], 0, s[64:65]
	v_lshl_add_u64 v[216:217], v[206:207], 0, s[64:65]
	v_lshl_add_u64 v[222:223], v[208:209], 0, s[64:65]
	v_lshl_add_u64 v[224:225], v[210:211], 0, s[64:65]
	s_lshl_b32 s64, s14, 16
	s_add_i32 s14, s18, s16
	s_waitcnt lgkmcnt(0)
	s_barrier
	s_cmp_lt_u32 s13, 62
	s_cbranch_scc0 .Lskipv_53694
	s_cmp_eq_u32 s55, 0
	s_cbranch_scc0 .Lstg_a53694
	v_lshl_add_u64 v[180:181], v[212:213], 0, s[64:65]
	s_mov_b32 m0, s14
	global_load_dwordx4 v[184:187], v[180:181], off nt
	s_nop 0
	global_load_dwordx4 v[180:183], v[180:181], off offset:2048 nt
	s_nop 0
	global_load_lds_dwordx4 v[196:197], off
	s_add_i32 m0, s14, 0x400
	s_nop 0
	global_load_lds_dwordx4 v[198:199], off
	s_add_i32 m0, s14, 0x800
	s_nop 0
	global_load_lds_dwordx4 v[216:217], off
	s_add_i32 m0, s14, 0xc00
	s_nop 0
	global_load_lds_dwordx4 v[222:223], off
	s_add_i32 m0, s14, 0x1000
	s_nop 0
	global_load_lds_dwordx4 v[224:225], off
.Lstg_a53694:
.Lskipv_53694:
	v_add_u32_e32 v216, s15, v86
	ds_read2_b32 v[196:197], v233 offset0:0 offset1:0x84
	ds_read2_b32 v[198:199], v234 offset0:0 offset1:0x84
	ds_read2_b32 v[222:223], v233 offset0:16 offset1:0x94
	ds_read2_b32 v[224:225], v234 offset0:16 offset1:0x94
	ds_read2_b32 v[226:227], v233 offset0:32 offset1:0xa4
	ds_read2_b32 v[228:229], v234 offset0:32 offset1:0xa4
	ds_read2_b32 v[238:239], v233 offset0:48 offset1:0xb4
	ds_read2_b32 v[240:241], v234 offset0:48 offset1:0xb4
	ds_read_b128 v[242:245], v216 offset:0
	ds_read_b128 v[246:249], v216 offset:0x400
	s_nop 0
	s_waitcnt lgkmcnt(1)
	s_setprio 1
	v_mfma_f32_16x16x32_bf16 v[140:143], v[196:199], v[242:245], v[140:143]
	v_mfma_f32_16x16x32_bf16 v[132:135], v[222:225], v[242:245], v[132:135]
	v_mfma_f32_16x16x32_bf16 v[144:147], v[226:229], v[242:245], v[144:147]
	v_mfma_f32_16x16x32_bf16 v[136:139], v[238:241], v[242:245], v[136:139]
	ds_read_b128 v[242:245], v216 offset:0x800
	s_waitcnt lgkmcnt(1)
	s_nop 0
	v_mfma_f32_16x16x32_bf16 v[124:127], v[196:199], v[246:249], v[124:127]
	v_mfma_f32_16x16x32_bf16 v[112:115], v[222:225], v[246:249], v[112:115]
	v_mfma_f32_16x16x32_bf16 v[128:131], v[226:229], v[246:249], v[128:131]
	v_mfma_f32_16x16x32_bf16 v[116:119], v[238:241], v[246:249], v[116:119]
	ds_read_b128 v[246:249], v216 offset:0xc00
	s_waitcnt lgkmcnt(1)
	s_nop 0
	v_mfma_f32_16x16x32_bf16 v[82:85], v[196:199], v[242:245], v[82:85]
	v_mfma_f32_16x16x32_bf16 v[54:57], v[222:225], v[242:245], v[54:57]
	v_mfma_f32_16x16x32_bf16 v[88:91], v[226:229], v[242:245], v[88:91]
	v_mfma_f32_16x16x32_bf16 v[58:61], v[238:241], v[242:245], v[58:61]
	ds_read_b128 v[242:245], v216 offset:0x1000
	s_waitcnt lgkmcnt(1)
	s_nop 0
	v_mfma_f32_16x16x32_bf16 v[26:29], v[196:199], v[246:249], v[26:29]
	v_mfma_f32_16x16x32_bf16 v[6:9], v[222:225], v[246:249], v[6:9]
	v_mfma_f32_16x16x32_bf16 v[42:45], v[226:229], v[246:249], v[42:45]
	v_mfma_f32_16x16x32_bf16 v[14:17], v[238:241], v[246:249], v[14:17]
	ds_read_b128 v[246:249], v216 offset:0x1400
	s_waitcnt lgkmcnt(1)
	s_nop 0
	v_mfma_f32_16x16x32_bf16 v[92:95], v[196:199], v[242:245], v[92:95]
	v_mfma_f32_16x16x32_bf16 v[62:65], v[222:225], v[242:245], v[62:65]
	v_mfma_f32_16x16x32_bf16 v[96:99], v[226:229], v[242:245], v[96:99]
	v_mfma_f32_16x16x32_bf16 v[66:69], v[238:241], v[242:245], v[66:69]
	ds_read_b128 v[242:245], v216 offset:0x1800
	s_waitcnt lgkmcnt(1)
	s_nop 0
	v_mfma_f32_16x16x32_bf16 v[38:41], v[196:199], v[246:249], v[38:41]
	v_mfma_f32_16x16x32_bf16 v[18:21], v[222:225], v[246:249], v[18:21]
	v_mfma_f32_16x16x32_bf16 v[46:49], v[226:229], v[246:249], v[46:49]
	v_mfma_f32_16x16x32_bf16 v[22:25], v[238:241], v[246:249], v[22:25]
	ds_read_b128 v[246:249], v216 offset:0x1c00
	s_waitcnt lgkmcnt(1)
	s_nop 0
	v_mfma_f32_16x16x32_bf16 v[108:111], v[196:199], v[242:245], v[108:111]
	v_mfma_f32_16x16x32_bf16 v[100:103], v[222:225], v[242:245], v[100:103]
	v_mfma_f32_16x16x32_bf16 v[120:123], v[226:229], v[242:245], v[120:123]
	v_mfma_f32_16x16x32_bf16 v[104:107], v[238:241], v[242:245], v[104:107]
	ds_read_b128 v[242:245], v216 offset:0x2000
	s_waitcnt lgkmcnt(1)
	s_nop 0
	v_mfma_f32_16x16x32_bf16 v[70:73], v[196:199], v[246:249], v[70:73]
	v_mfma_f32_16x16x32_bf16 v[50:53], v[222:225], v[246:249], v[50:53]
	v_mfma_f32_16x16x32_bf16 v[10:13], v[226:229], v[246:249], v[10:13]
	v_mfma_f32_16x16x32_bf16 v[2:5], v[238:241], v[246:249], v[2:5]
	ds_read_b128 v[246:249], v216 offset:0x2400
	s_waitcnt lgkmcnt(1)
	s_nop 0
	v_mfma_f32_16x16x32_bf16 v[176:179], v[196:199], v[242:245], v[176:179]
	s_waitcnt lgkmcnt(0)
	v_mfma_f32_16x16x32_bf16 v[168:171], v[222:225], v[242:245], v[168:171]
	v_mfma_f32_16x16x32_bf16 v[172:175], v[226:229], v[242:245], v[172:175]
	v_mfma_f32_16x16x32_bf16 v[164:167], v[238:241], v[242:245], v[164:167]
	v_mfma_f32_16x16x32_bf16 v[160:163], v[196:199], v[246:249], v[160:163]
	v_mfma_f32_16x16x32_bf16 v[152:155], v[222:225], v[246:249], v[152:155]
	v_mfma_f32_16x16x32_bf16 v[156:159], v[226:229], v[246:249], v[156:159]
	v_mfma_f32_16x16x32_bf16 v[148:151], v[238:241], v[246:249], v[148:151]
	s_cmp_lt_u32 s13, 62
	s_cbranch_scc0 .Lstg_b53694
	s_cmp_eq_u32 s55, 0
	s_cbranch_scc1 .Lstg_b53694
	v_lshl_add_u64 v[180:181], v[212:213], 0, s[64:65]
	s_lshr_b32 s64, s64, 10
	v_lshl_add_u64 v[182:183], v[202:203], 0, s[64:65]
	s_mov_b32 m0, s14
	s_nop 0
	global_load_lds_dwordx4 v[182:183], off
	v_lshl_add_u64 v[182:183], v[204:205], 0, s[64:65]
	s_add_i32 m0, s14, 0x400
	s_nop 0
	global_load_lds_dwordx4 v[182:183], off
	v_lshl_add_u64 v[182:183], v[206:207], 0, s[64:65]
	s_add_i32 m0, s14, 0x800
	s_nop 0
	global_load_lds_dwordx4 v[182:183], off
	v_lshl_add_u64 v[182:183], v[208:209], 0, s[64:65]
	s_add_i32 m0, s14, 0xc00
	s_nop 0
	global_load_lds_dwordx4 v[182:183], off
	v_lshl_add_u64 v[182:183], v[210:211], 0, s[64:65]
	s_add_i32 m0, s14, 0x1000
	s_nop 0
	global_load_lds_dwordx4 v[182:183], off
	global_load_dwordx4 v[184:187], v[180:181], off nt
	s_nop 0
	global_load_dwordx4 v[180:183], v[180:181], off offset:2048 nt

.LBB0_3448:
	s_add_i32 s7, s8, 2
	s_add_i32 s8, s8, 4
	s_min_u32 s8, s8, 15
	s_mul_i32 s9, s6, 0xa000
	s_lshl_b32 s64, s8, 6
	s_add_i32 s24, s9, 0xffff6000
	s_cmp_lg_u32 s6, 0
	s_cselect_b32 s24, s24, 0x14000
	s_add_i32 s24, s22, s24
	s_waitcnt lgkmcnt(0)
	s_barrier
	s_cmp_lt_u32 s7, 14
	s_cbranch_scc0 .Lskipv_56180
	s_cmp_eq_u32 s55, 0
	s_cbranch_scc0 .Lstg_a56180
	v_lshl_add_u64 v[156:157], v[200:201], 0, s[64:65]
	s_mov_b32 m0, s24
	s_nop 0
	global_load_lds_dwordx4 v[156:157], off
	v_lshl_add_u64 v[156:157], v[202:203], 0, s[64:65]
	s_add_i32 m0, s24, 0x400
	s_nop 0
	global_load_lds_dwordx4 v[156:157], off
	v_lshl_add_u64 v[156:157], v[204:205], 0, s[64:65]
	s_add_i32 m0, s24, 0x800
	s_nop 0
	global_load_lds_dwordx4 v[156:157], off
	v_lshl_add_u64 v[156:157], v[206:207], 0, s[64:65]
	s_add_i32 m0, s24, 0xc00
	s_nop 0
	global_load_lds_dwordx4 v[156:157], off
	v_lshl_add_u64 v[156:157], v[208:209], 0, s[64:65]
	s_add_i32 m0, s24, 0x1000
	s_lshl_b32 s64, s8, 18
	global_load_lds_dwordx4 v[156:157], off
	v_lshl_add_u64 v[156:157], v[210:211], 0, s[64:65]
	v_add_co_u32_e32 v160, vcc, s33, v156
	s_nop 1
	v_addc_co_u32_e32 v161, vcc, 0, v157, vcc
	global_load_dwordx4 v[156:159], v[156:157], off nt
	s_nop 0
	global_load_dwordx4 v[160:163], v[160:161], off nt
.Lstg_a56180:
.Lskipv_56180:
	v_add_u32_e32 v167, s9, v86
	ds_read2_b32 v[168:169], v232 offset0:0 offset1:0x84
	ds_read2_b32 v[170:171], v233 offset0:0 offset1:0x84
	ds_read2_b32 v[172:173], v232 offset0:16 offset1:0x94
	ds_read2_b32 v[174:175], v233 offset0:16 offset1:0x94
	ds_read2_b32 v[176:177], v232 offset0:32 offset1:0xa4
	ds_read2_b32 v[178:179], v233 offset0:32 offset1:0xa4
	ds_read2_b32 v[180:181], v232 offset0:48 offset1:0xb4
	ds_read2_b32 v[182:183], v233 offset0:48 offset1:0xb4
	ds_read_b128 v[184:187], v167 offset:0
	ds_read_b128 v[188:191], v167 offset:0x400
	s_nop 0
	s_waitcnt lgkmcnt(1)
	s_setprio 1
	v_mfma_f32_16x16x32_bf16 v[78:81], v[168:171], v[184:187], v[78:81]
	v_mfma_f32_16x16x32_bf16 v[74:77], v[172:175], v[184:187], v[74:77]
	v_mfma_f32_16x16x32_bf16 v[70:73], v[176:179], v[184:187], v[70:73]
	v_mfma_f32_16x16x32_bf16 v[66:69], v[180:183], v[184:187], v[66:69]
	ds_read_b128 v[184:187], v167 offset:0x800
	s_waitcnt lgkmcnt(1)
	s_nop 0
	v_mfma_f32_16x16x32_bf16 v[62:65], v[168:171], v[188:191], v[62:65]
	v_mfma_f32_16x16x32_bf16 v[58:61], v[172:175], v[188:191], v[58:61]
	v_mfma_f32_16x16x32_bf16 v[54:57], v[176:179], v[188:191], v[54:57]
	v_mfma_f32_16x16x32_bf16 v[50:53], v[180:183], v[188:191], v[50:53]
	ds_read_b128 v[188:191], v167 offset:0xc00
	s_waitcnt lgkmcnt(1)
	s_nop 0
	v_mfma_f32_16x16x32_bf16 v[46:49], v[168:171], v[184:187], v[46:49]
	v_mfma_f32_16x16x32_bf16 v[42:45], v[172:175], v[184:187], v[42:45]
	v_mfma_f32_16x16x32_bf16 v[38:41], v[176:179], v[184:187], v[38:41]
	v_mfma_f32_16x16x32_bf16 v[34:37], v[180:183], v[184:187], v[34:37]
	ds_read_b128 v[184:187], v167 offset:0x1000
	s_waitcnt lgkmcnt(1)
	s_nop 0
	v_mfma_f32_16x16x32_bf16 v[18:21], v[168:171], v[188:191], v[18:21]
	v_mfma_f32_16x16x32_bf16 v[22:25], v[172:175], v[188:191], v[22:25]
	v_mfma_f32_16x16x32_bf16 v[26:29], v[176:179], v[188:191], v[26:29]
	v_mfma_f32_16x16x32_bf16 v[30:33], v[180:183], v[188:191], v[30:33]
	ds_read_b128 v[188:191], v167 offset:0x1400
	s_waitcnt lgkmcnt(1)
	s_nop 0
	v_mfma_f32_16x16x32_bf16 v[88:91], v[168:171], v[184:187], v[88:91]
	v_mfma_f32_16x16x32_bf16 v[112:115], v[172:175], v[184:187], v[112:115]
	v_mfma_f32_16x16x32_bf16 v[108:111], v[176:179], v[184:187], v[108:111]
	v_mfma_f32_16x16x32_bf16 v[100:103], v[180:183], v[184:187], v[100:103]
	ds_read_b128 v[184:187], v167 offset:0x1800
	s_waitcnt lgkmcnt(1)
	s_nop 0
	v_mfma_f32_16x16x32_bf16 v[82:85], v[168:171], v[188:191], v[82:85]
	v_mfma_f32_16x16x32_bf16 v[92:95], v[172:175], v[188:191], v[92:95]
	v_mfma_f32_16x16x32_bf16 v[96:99], v[176:179], v[188:191], v[96:99]
	v_mfma_f32_16x16x32_bf16 v[104:107], v[180:183], v[188:191], v[104:107]
	ds_read_b128 v[188:191], v167 offset:0x1c00
	s_waitcnt lgkmcnt(1)
	s_nop 0
	v_mfma_f32_16x16x32_bf16 v[116:119], v[168:171], v[184:187], v[116:119]
	s_waitcnt lgkmcnt(0)
	v_mfma_f32_16x16x32_bf16 v[124:127], v[172:175], v[184:187], v[124:127]
	v_mfma_f32_16x16x32_bf16 v[132:135], v[176:179], v[184:187], v[132:135]
	v_mfma_f32_16x16x32_bf16 v[136:139], v[180:183], v[184:187], v[136:139]
	v_mfma_f32_16x16x32_bf16 v[120:123], v[168:171], v[188:191], v[120:123]
	v_mfma_f32_16x16x32_bf16 v[128:131], v[172:175], v[188:191], v[128:131]
	v_mfma_f32_16x16x32_bf16 v[140:143], v[176:179], v[188:191], v[140:143]
	v_mfma_f32_16x16x32_bf16 v[144:147], v[180:183], v[188:191], v[144:147]
	s_cmp_lt_u32 s7, 14
	s_cbranch_scc0 .Lstg_b56180
	s_cmp_eq_u32 s55, 0
	s_cbranch_scc1 .Lstg_b56180
	v_lshl_add_u64 v[156:157], v[200:201], 0, s[64:65]
	s_mov_b32 m0, s24
	s_nop 0
	global_load_lds_dwordx4 v[156:157], off
	v_lshl_add_u64 v[156:157], v[202:203], 0, s[64:65]
	s_add_i32 m0, s24, 0x400
	s_nop 0
	global_load_lds_dwordx4 v[156:157], off
	v_lshl_add_u64 v[156:157], v[204:205], 0, s[64:65]
	s_add_i32 m0, s24, 0x800
	s_nop 0
	global_load_lds_dwordx4 v[156:157], off
	v_lshl_add_u64 v[156:157], v[206:207], 0, s[64:65]
	s_add_i32 m0, s24, 0xc00
	s_nop 0
	global_load_lds_dwordx4 v[156:157], off
	v_lshl_add_u64 v[156:157], v[208:209], 0, s[64:65]
	s_add_i32 m0, s24, 0x1000
	s_lshl_b32 s64, s8, 18
	global_load_lds_dwordx4 v[156:157], off
	v_lshl_add_u64 v[156:157], v[210:211], 0, s[64:65]
	v_add_co_u32_e32 v160, vcc, s33, v156
	s_nop 1
	v_addc_co_u32_e32 v161, vcc, 0, v157, vcc
	global_load_dwordx4 v[156:159], v[156:157], off nt
	s_nop 0
	global_load_dwordx4 v[160:163], v[160:161], off nt
.Lstg_b56180:
	s_setprio 0
	s_cmp_lt_u32 s7, 14
	s_cbranch_scc1 .Lokw_56180
	s_waitcnt vmcnt(0)
.Lokw_56180:
	s_add_i32 s8, s6, 1
	s_cmp_lg_u32 s6, 2
	s_cselect_b32 s6, s8, 0
	s_min_u32 s8, s7, 12
	s_add_i32 s8, s8, 3
	s_mul_i32 s9, s6, 0xa000
	s_lshl_b32 s64, s8, 6
	s_add_i32 s24, s9, 0xffff6000
	s_cmp_lg_u32 s6, 0
	s_waitcnt vmcnt(7)
	v_cvt_pk_bf16_f32 v148, v148, v152
	v_add_u32_e32 v152, 0x20100, v165
	s_cselect_b32 s24, s24, 0x14000
	v_cvt_pk_bf16_f32 v149, v149, v153
	v_cvt_pk_bf16_f32 v150, v150, v154
	v_cvt_pk_bf16_f32 v151, v151, v155
	ds_write_b128 v152, v[148:151]
	s_add_i32 s24, s22, s24
	s_waitcnt lgkmcnt(0)
	s_barrier
	s_cmp_lt_u32 s7, 14
	s_cbranch_scc0 .Lskipv_56354
	s_cmp_eq_u32 s55, 0
	s_cbranch_scc0 .Lstg_a56354
	v_lshl_add_u64 v[148:149], v[200:201], 0, s[64:65]
	s_mov_b32 m0, s24
	s_nop 0
	global_load_lds_dwordx4 v[148:149], off
	v_lshl_add_u64 v[148:149], v[202:203], 0, s[64:65]
	s_add_i32 m0, s24, 0x400
	s_nop 0
	global_load_lds_dwordx4 v[148:149], off
	v_lshl_add_u64 v[148:149], v[204:205], 0, s[64:65]
	s_add_i32 m0, s24, 0x800
	s_nop 0
	global_load_lds_dwordx4 v[148:149], off
	v_lshl_add_u64 v[148:149], v[206:207], 0, s[64:65]
	s_add_i32 m0, s24, 0xc00
	s_nop 0
	global_load_lds_dwordx4 v[148:149], off
	v_lshl_add_u64 v[148:149], v[208:209], 0, s[64:65]
	s_lshl_b32 s64, s8, 18
	s_add_i32 m0, s24, 0x1000
	v_lshl_add_u64 v[152:153], v[210:211], 0, s[64:65]
	global_load_lds_dwordx4 v[148:149], off
	global_load_dwordx4 v[148:151], v[152:153], off nt
	v_add_co_u32_e32 v152, vcc, s33, v152
	s_nop 1
	v_addc_co_u32_e32 v153, vcc, 0, v153, vcc
	global_load_dwordx4 v[152:155], v[152:153], off nt
.Lstg_a56354:
.Lskipv_56354:
	v_add_u32_e32 v167, s9, v86
	ds_read2_b32 v[168:169], v234 offset0:0 offset1:0x84
	ds_read2_b32 v[170:171], v235 offset0:0 offset1:0x84
	ds_read2_b32 v[172:173], v234 offset0:16 offset1:0x94
	ds_read2_b32 v[174:175], v235 offset0:16 offset1:0x94
	ds_read2_b32 v[176:177], v234 offset0:32 offset1:0xa4
	ds_read2_b32 v[178:179], v235 offset0:32 offset1:0xa4
	ds_read2_b32 v[180:181], v234 offset0:48 offset1:0xb4
	ds_read2_b32 v[182:183], v235 offset0:48 offset1:0xb4
	ds_read_b128 v[184:187], v167 offset:0
	ds_read_b128 v[188:191], v167 offset:0x400
	s_nop 0
	s_waitcnt lgkmcnt(1)
	s_setprio 1
	v_mfma_f32_16x16x32_bf16 v[78:81], v[168:171], v[184:187], v[78:81]
	v_mfma_f32_16x16x32_bf16 v[74:77], v[172:175], v[184:187], v[74:77]
	v_mfma_f32_16x16x32_bf16 v[70:73], v[176:179], v[184:187], v[70:73]
	v_mfma_f32_16x16x32_bf16 v[66:69], v[180:183], v[184:187], v[66:69]
	ds_read_b128 v[184:187], v167 offset:0x800
	s_waitcnt lgkmcnt(1)
	s_nop 0
	v_mfma_f32_16x16x32_bf16 v[62:65], v[168:171], v[188:191], v[62:65]
	v_mfma_f32_16x16x32_bf16 v[58:61], v[172:175], v[188:191], v[58:61]
	v_mfma_f32_16x16x32_bf16 v[54:57], v[176:179], v[188:191], v[54:57]
	v_mfma_f32_16x16x32_bf16 v[50:53], v[180:183], v[188:191], v[50:53]
	ds_read_b128 v[188:191], v167 offset:0xc00
	s_waitcnt lgkmcnt(1)
	s_nop 0
	v_mfma_f32_16x16x32_bf16 v[46:49], v[168:171], v[184:187], v[46:49]
	v_mfma_f32_16x16x32_bf16 v[42:45], v[172:175], v[184:187], v[42:45]
	v_mfma_f32_16x16x32_bf16 v[38:41], v[176:179], v[184:187], v[38:41]
	v_mfma_f32_16x16x32_bf16 v[34:37], v[180:183], v[184:187], v[34:37]
	ds_read_b128 v[184:187], v167 offset:0x1000
	s_waitcnt lgkmcnt(1)
	s_nop 0
	v_mfma_f32_16x16x32_bf16 v[18:21], v[168:171], v[188:191], v[18:21]
	v_mfma_f32_16x16x32_bf16 v[22:25], v[172:175], v[188:191], v[22:25]
	v_mfma_f32_16x16x32_bf16 v[26:29], v[176:179], v[188:191], v[26:29]
	v_mfma_f32_16x16x32_bf16 v[30:33], v[180:183], v[188:191], v[30:33]
	ds_read_b128 v[188:191], v167 offset:0x1400
	s_waitcnt lgkmcnt(1)
	s_nop 0
	v_mfma_f32_16x16x32_bf16 v[88:91], v[168:171], v[184:187], v[88:91]
	v_mfma_f32_16x16x32_bf16 v[112:115], v[172:175], v[184:187], v[112:115]
	v_mfma_f32_16x16x32_bf16 v[108:111], v[176:179], v[184:187], v[108:111]
	v_mfma_f32_16x16x32_bf16 v[100:103], v[180:183], v[184:187], v[100:103]
	ds_read_b128 v[184:187], v167 offset:0x1800
	s_waitcnt lgkmcnt(1)
	s_nop 0
	v_mfma_f32_16x16x32_bf16 v[82:85], v[168:171], v[188:191], v[82:85]
	v_mfma_f32_16x16x32_bf16 v[92:95], v[172:175], v[188:191], v[92:95]
	v_mfma_f32_16x16x32_bf16 v[96:99], v[176:179], v[188:191], v[96:99]
	v_mfma_f32_16x16x32_bf16 v[104:107], v[180:183], v[188:191], v[104:107]
	ds_read_b128 v[188:191], v167 offset:0x1c00
	s_waitcnt lgkmcnt(1)
	s_nop 0
	v_mfma_f32_16x16x32_bf16 v[116:119], v[168:171], v[184:187], v[116:119]
	s_waitcnt lgkmcnt(0)
	v_mfma_f32_16x16x32_bf16 v[124:127], v[172:175], v[184:187], v[124:127]
	v_mfma_f32_16x16x32_bf16 v[132:135], v[176:179], v[184:187], v[132:135]
	v_mfma_f32_16x16x32_bf16 v[136:139], v[180:183], v[184:187], v[136:139]
	v_mfma_f32_16x16x32_bf16 v[120:123], v[168:171], v[188:191], v[120:123]
	v_mfma_f32_16x16x32_bf16 v[128:131], v[172:175], v[188:191], v[128:131]
	v_mfma_f32_16x16x32_bf16 v[140:143], v[176:179], v[188:191], v[140:143]
	v_mfma_f32_16x16x32_bf16 v[144:147], v[180:183], v[188:191], v[144:147]
	s_cmp_lt_u32 s7, 14
	s_cbranch_scc0 .Lstg_b56354
	s_cmp_eq_u32 s55, 0
	s_cbranch_scc1 .Lstg_b56354
	v_lshl_add_u64 v[148:149], v[200:201], 0, s[64:65]
	s_mov_b32 m0, s24
	s_nop 0
	global_load_lds_dwordx4 v[148:149], off
	v_lshl_add_u64 v[148:149], v[202:203], 0, s[64:65]
	s_add_i32 m0, s24, 0x400
	s_nop 0
	global_load_lds_dwordx4 v[148:149], off
	v_lshl_add_u64 v[148:149], v[204:205], 0, s[64:65]
	s_add_i32 m0, s24, 0x800
	s_nop 0
	global_load_lds_dwordx4 v[148:149], off
	v_lshl_add_u64 v[148:149], v[206:207], 0, s[64:65]
	s_add_i32 m0, s24, 0xc00
	s_nop 0
	global_load_lds_dwordx4 v[148:149], off
	v_lshl_add_u64 v[148:149], v[208:209], 0, s[64:65]
	s_lshl_b32 s64, s8, 18
	s_add_i32 m0, s24, 0x1000
	v_lshl_add_u64 v[152:153], v[210:211], 0, s[64:65]
	global_load_lds_dwordx4 v[148:149], off
	global_load_dwordx4 v[148:151], v[152:153], off nt
	v_add_co_u32_e32 v152, vcc, s33, v152
	s_nop 1
	v_addc_co_u32_e32 v153, vcc, 0, v153, vcc
	global_load_dwordx4 v[152:155], v[152:153], off nt

.LBB0_3466:
	s_add_i32 s5, s6, 2
	s_add_i32 s6, s6, 4
	s_min_u32 s6, s6, 15
	s_mul_i32 s7, s4, 0xa000
	s_lshl_b32 s64, s6, 6
	s_add_i32 s8, s7, 0xffff6000
	s_cmp_lg_u32 s4, 0
	s_cselect_b32 s8, s8, 0x14000
	s_add_i32 s8, s22, s8
	s_waitcnt lgkmcnt(0)
	s_barrier
	s_cmp_lt_u32 s5, 14
	s_cbranch_scc0 .Lskipv_57720
	s_cmp_eq_u32 s55, 0
	s_cbranch_scc0 .Lstg_a57720
	v_lshl_add_u64 v[188:189], v[200:201], 0, s[64:65]
	s_mov_b32 m0, s8
	s_nop 0
	global_load_lds_dwordx4 v[188:189], off
	v_lshl_add_u64 v[188:189], v[202:203], 0, s[64:65]
	s_add_i32 m0, s8, 0x400
	s_nop 0
	global_load_lds_dwordx4 v[188:189], off
	v_lshl_add_u64 v[188:189], v[204:205], 0, s[64:65]
	s_add_i32 m0, s8, 0x800
	s_nop 0
	global_load_lds_dwordx4 v[188:189], off
	v_lshl_add_u64 v[188:189], v[206:207], 0, s[64:65]
	s_add_i32 m0, s8, 0xc00
	s_nop 0
	global_load_lds_dwordx4 v[188:189], off
	v_lshl_add_u64 v[188:189], v[208:209], 0, s[64:65]
	s_add_i32 m0, s8, 0x1000
	s_lshl_b32 s64, s6, 18
	global_load_lds_dwordx4 v[188:189], off
	v_lshl_add_u64 v[188:189], v[210:211], 0, s[64:65]
	v_add_co_u32_e32 v192, vcc, s33, v188
	s_nop 1
	v_addc_co_u32_e32 v193, vcc, 0, v189, vcc
	global_load_dwordx4 v[188:191], v[188:189], off nt
	s_nop 0
	global_load_dwordx4 v[192:195], v[192:193], off nt
.Lstg_a57720:
.Lskipv_57720:
	v_add_u32_e32 v216, s7, v86
	ds_read2_b32 v[196:197], v232 offset0:0 offset1:0x84
	ds_read2_b32 v[198:199], v233 offset0:0 offset1:0x84
	ds_read2_b32 v[222:223], v232 offset0:16 offset1:0x94
	ds_read2_b32 v[224:225], v233 offset0:16 offset1:0x94
	ds_read2_b32 v[226:227], v232 offset0:32 offset1:0xa4
	ds_read2_b32 v[228:229], v233 offset0:32 offset1:0xa4
	ds_read2_b32 v[238:239], v232 offset0:48 offset1:0xb4
	ds_read2_b32 v[240:241], v233 offset0:48 offset1:0xb4
	ds_read_b128 v[242:245], v216 offset:0
	ds_read_b128 v[246:249], v216 offset:0x400
	s_nop 0
	s_waitcnt lgkmcnt(1)
	s_setprio 1
	v_mfma_f32_16x16x32_bf16 v[78:81], v[196:199], v[242:245], v[78:81]
	v_mfma_f32_16x16x32_bf16 v[74:77], v[222:225], v[242:245], v[74:77]
	v_mfma_f32_16x16x32_bf16 v[70:73], v[226:229], v[242:245], v[70:73]
	v_mfma_f32_16x16x32_bf16 v[66:69], v[238:241], v[242:245], v[66:69]
	ds_read_b128 v[242:245], v216 offset:0x800
	s_waitcnt lgkmcnt(1)
	s_nop 0
	v_mfma_f32_16x16x32_bf16 v[62:65], v[196:199], v[246:249], v[62:65]
	v_mfma_f32_16x16x32_bf16 v[58:61], v[222:225], v[246:249], v[58:61]
	v_mfma_f32_16x16x32_bf16 v[54:57], v[226:229], v[246:249], v[54:57]
	v_mfma_f32_16x16x32_bf16 v[50:53], v[238:241], v[246:249], v[50:53]
	ds_read_b128 v[246:249], v216 offset:0xc00
	s_waitcnt lgkmcnt(1)
	s_nop 0
	v_mfma_f32_16x16x32_bf16 v[46:49], v[196:199], v[242:245], v[46:49]
	v_mfma_f32_16x16x32_bf16 v[42:45], v[222:225], v[242:245], v[42:45]
	v_mfma_f32_16x16x32_bf16 v[38:41], v[226:229], v[242:245], v[38:41]
	v_mfma_f32_16x16x32_bf16 v[34:37], v[238:241], v[242:245], v[34:37]
	ds_read_b128 v[242:245], v216 offset:0x1000
	s_waitcnt lgkmcnt(1)
	s_nop 0
	v_mfma_f32_16x16x32_bf16 v[18:21], v[196:199], v[246:249], v[18:21]
	v_mfma_f32_16x16x32_bf16 v[22:25], v[222:225], v[246:249], v[22:25]
	v_mfma_f32_16x16x32_bf16 v[26:29], v[226:229], v[246:249], v[26:29]
	v_mfma_f32_16x16x32_bf16 v[30:33], v[238:241], v[246:249], v[30:33]
	ds_read_b128 v[246:249], v216 offset:0x1400
	s_waitcnt lgkmcnt(1)
	s_nop 0
	v_mfma_f32_16x16x32_bf16 v[88:91], v[196:199], v[242:245], v[88:91]
	v_mfma_f32_16x16x32_bf16 v[112:115], v[222:225], v[242:245], v[112:115]
	v_mfma_f32_16x16x32_bf16 v[108:111], v[226:229], v[242:245], v[108:111]
	v_mfma_f32_16x16x32_bf16 v[100:103], v[238:241], v[242:245], v[100:103]
	ds_read_b128 v[242:245], v216 offset:0x1800
	s_waitcnt lgkmcnt(1)
	s_nop 0
	v_mfma_f32_16x16x32_bf16 v[82:85], v[196:199], v[246:249], v[82:85]
	v_mfma_f32_16x16x32_bf16 v[92:95], v[222:225], v[246:249], v[92:95]
	v_mfma_f32_16x16x32_bf16 v[96:99], v[226:229], v[246:249], v[96:99]
	v_mfma_f32_16x16x32_bf16 v[104:107], v[238:241], v[246:249], v[104:107]
	ds_read_b128 v[246:249], v216 offset:0x1c00
	s_waitcnt lgkmcnt(1)
	s_nop 0
	v_mfma_f32_16x16x32_bf16 v[116:119], v[196:199], v[242:245], v[116:119]
	v_mfma_f32_16x16x32_bf16 v[124:127], v[222:225], v[242:245], v[124:127]
	v_mfma_f32_16x16x32_bf16 v[132:135], v[226:229], v[242:245], v[132:135]
	v_mfma_f32_16x16x32_bf16 v[136:139], v[238:241], v[242:245], v[136:139]
	ds_read_b128 v[242:245], v216 offset:0x2000
	s_waitcnt lgkmcnt(1)
	s_nop 0
	v_mfma_f32_16x16x32_bf16 v[120:123], v[196:199], v[246:249], v[120:123]
	v_mfma_f32_16x16x32_bf16 v[128:131], v[222:225], v[246:249], v[128:131]
	v_mfma_f32_16x16x32_bf16 v[140:143], v[226:229], v[246:249], v[140:143]
	v_mfma_f32_16x16x32_bf16 v[144:147], v[238:241], v[246:249], v[144:147]
	ds_read_b128 v[246:249], v216 offset:0x2400
	s_waitcnt lgkmcnt(1)
	s_nop 0
	v_mfma_f32_16x16x32_bf16 v[148:151], v[196:199], v[242:245], v[148:151]
	s_waitcnt lgkmcnt(0)
	v_mfma_f32_16x16x32_bf16 v[176:179], v[222:225], v[242:245], v[176:179]
	v_mfma_f32_16x16x32_bf16 v[172:175], v[226:229], v[242:245], v[172:175]
	v_mfma_f32_16x16x32_bf16 v[168:171], v[238:241], v[242:245], v[168:171]
	v_mfma_f32_16x16x32_bf16 v[164:167], v[196:199], v[246:249], v[164:167]
	v_mfma_f32_16x16x32_bf16 v[160:163], v[222:225], v[246:249], v[160:163]
	v_mfma_f32_16x16x32_bf16 v[156:159], v[226:229], v[246:249], v[156:159]
	v_mfma_f32_16x16x32_bf16 v[152:155], v[238:241], v[246:249], v[152:155]
	s_cmp_lt_u32 s5, 14
	s_cbranch_scc0 .Lstg_b57720
	s_cmp_eq_u32 s55, 0
	s_cbranch_scc1 .Lstg_b57720
	v_lshl_add_u64 v[188:189], v[200:201], 0, s[64:65]
	s_mov_b32 m0, s8
	s_nop 0
	global_load_lds_dwordx4 v[188:189], off
	v_lshl_add_u64 v[188:189], v[202:203], 0, s[64:65]
	s_add_i32 m0, s8, 0x400
	s_nop 0
	global_load_lds_dwordx4 v[188:189], off
	v_lshl_add_u64 v[188:189], v[204:205], 0, s[64:65]
	s_add_i32 m0, s8, 0x800
	s_nop 0
	global_load_lds_dwordx4 v[188:189], off
	v_lshl_add_u64 v[188:189], v[206:207], 0, s[64:65]
	s_add_i32 m0, s8, 0xc00
	s_nop 0
	global_load_lds_dwordx4 v[188:189], off
	v_lshl_add_u64 v[188:189], v[208:209], 0, s[64:65]
	s_add_i32 m0, s8, 0x1000
	s_lshl_b32 s64, s6, 18
	global_load_lds_dwordx4 v[188:189], off
	v_lshl_add_u64 v[188:189], v[210:211], 0, s[64:65]
	v_add_co_u32_e32 v192, vcc, s33, v188
	s_nop 1
	v_addc_co_u32_e32 v193, vcc, 0, v189, vcc
	global_load_dwordx4 v[188:191], v[188:189], off nt
	s_nop 0
	global_load_dwordx4 v[192:195], v[192:193], off nt
.Lstg_b57720:
	s_setprio 0
	s_cmp_lt_u32 s5, 14
	s_cbranch_scc1 .Lokw_57720
	s_waitcnt vmcnt(0)
.Lokw_57720:
	s_add_i32 s6, s4, 1
	s_cmp_lg_u32 s4, 2
	s_cselect_b32 s4, s6, 0
	s_min_u32 s6, s5, 12
	s_add_i32 s6, s6, 3
	s_mul_i32 s7, s4, 0xa000
	s_lshl_b32 s64, s6, 6
	s_add_i32 s8, s7, 0xffff6000
	s_cmp_lg_u32 s4, 0
	s_waitcnt vmcnt(7)
	v_cvt_pk_bf16_f32 v180, v180, v184
	v_add_u32_e32 v184, 0x20100, v236
	s_cselect_b32 s8, s8, 0x14000
	v_cvt_pk_bf16_f32 v181, v181, v185
	v_cvt_pk_bf16_f32 v182, v182, v186
	v_cvt_pk_bf16_f32 v183, v183, v187
	ds_write_b128 v184, v[180:183]
	s_add_i32 s8, s22, s8
	s_waitcnt lgkmcnt(0)
	s_barrier
	s_cmp_lt_u32 s5, 14
	s_cbranch_scc0 .Lskipv_57916
	s_cmp_eq_u32 s55, 0
	s_cbranch_scc0 .Lstg_a57916
	v_lshl_add_u64 v[180:181], v[200:201], 0, s[64:65]
	s_mov_b32 m0, s8
	s_nop 0
	global_load_lds_dwordx4 v[180:181], off
	v_lshl_add_u64 v[180:181], v[202:203], 0, s[64:65]
	s_add_i32 m0, s8, 0x400
	s_nop 0
	global_load_lds_dwordx4 v[180:181], off
	v_lshl_add_u64 v[180:181], v[204:205], 0, s[64:65]
	s_add_i32 m0, s8, 0x800
	s_nop 0
	global_load_lds_dwordx4 v[180:181], off
	v_lshl_add_u64 v[180:181], v[206:207], 0, s[64:65]
	s_add_i32 m0, s8, 0xc00
	s_nop 0
	global_load_lds_dwordx4 v[180:181], off
	v_lshl_add_u64 v[180:181], v[208:209], 0, s[64:65]
	s_lshl_b32 s64, s6, 18
	s_add_i32 m0, s8, 0x1000
	v_lshl_add_u64 v[184:185], v[210:211], 0, s[64:65]
	global_load_lds_dwordx4 v[180:181], off
	global_load_dwordx4 v[180:183], v[184:185], off nt
	v_add_co_u32_e32 v184, vcc, s33, v184
	s_nop 1
	v_addc_co_u32_e32 v185, vcc, 0, v185, vcc
	global_load_dwordx4 v[184:187], v[184:185], off nt
.Lstg_a57916:
.Lskipv_57916:
	v_add_u32_e32 v216, s7, v86
	ds_read2_b32 v[196:197], v234 offset0:0 offset1:0x84
	ds_read2_b32 v[198:199], v235 offset0:0 offset1:0x84
	ds_read2_b32 v[222:223], v234 offset0:16 offset1:0x94
	ds_read2_b32 v[224:225], v235 offset0:16 offset1:0x94
	ds_read2_b32 v[226:227], v234 offset0:32 offset1:0xa4
	ds_read2_b32 v[228:229], v235 offset0:32 offset1:0xa4
	ds_read2_b32 v[238:239], v234 offset0:48 offset1:0xb4
	ds_read2_b32 v[240:241], v235 offset0:48 offset1:0xb4
	ds_read_b128 v[242:245], v216 offset:0
	ds_read_b128 v[246:249], v216 offset:0x400
	s_nop 0
	s_waitcnt lgkmcnt(1)
	s_setprio 1
	v_mfma_f32_16x16x32_bf16 v[78:81], v[196:199], v[242:245], v[78:81]
	v_mfma_f32_16x16x32_bf16 v[74:77], v[222:225], v[242:245], v[74:77]
	v_mfma_f32_16x16x32_bf16 v[70:73], v[226:229], v[242:245], v[70:73]
	v_mfma_f32_16x16x32_bf16 v[66:69], v[238:241], v[242:245], v[66:69]
	ds_read_b128 v[242:245], v216 offset:0x800
	s_waitcnt lgkmcnt(1)
	s_nop 0
	v_mfma_f32_16x16x32_bf16 v[62:65], v[196:199], v[246:249], v[62:65]
	v_mfma_f32_16x16x32_bf16 v[58:61], v[222:225], v[246:249], v[58:61]
	v_mfma_f32_16x16x32_bf16 v[54:57], v[226:229], v[246:249], v[54:57]
	v_mfma_f32_16x16x32_bf16 v[50:53], v[238:241], v[246:249], v[50:53]
	ds_read_b128 v[246:249], v216 offset:0xc00
	s_waitcnt lgkmcnt(1)
	s_nop 0
	v_mfma_f32_16x16x32_bf16 v[46:49], v[196:199], v[242:245], v[46:49]
	v_mfma_f32_16x16x32_bf16 v[42:45], v[222:225], v[242:245], v[42:45]
	v_mfma_f32_16x16x32_bf16 v[38:41], v[226:229], v[242:245], v[38:41]
	v_mfma_f32_16x16x32_bf16 v[34:37], v[238:241], v[242:245], v[34:37]
	ds_read_b128 v[242:245], v216 offset:0x1000
	s_waitcnt lgkmcnt(1)
	s_nop 0
	v_mfma_f32_16x16x32_bf16 v[18:21], v[196:199], v[246:249], v[18:21]
	v_mfma_f32_16x16x32_bf16 v[22:25], v[222:225], v[246:249], v[22:25]
	v_mfma_f32_16x16x32_bf16 v[26:29], v[226:229], v[246:249], v[26:29]
	v_mfma_f32_16x16x32_bf16 v[30:33], v[238:241], v[246:249], v[30:33]
	ds_read_b128 v[246:249], v216 offset:0x1400
	s_waitcnt lgkmcnt(1)
	s_nop 0
	v_mfma_f32_16x16x32_bf16 v[88:91], v[196:199], v[242:245], v[88:91]
	v_mfma_f32_16x16x32_bf16 v[112:115], v[222:225], v[242:245], v[112:115]
	v_mfma_f32_16x16x32_bf16 v[108:111], v[226:229], v[242:245], v[108:111]
	v_mfma_f32_16x16x32_bf16 v[100:103], v[238:241], v[242:245], v[100:103]
	ds_read_b128 v[242:245], v216 offset:0x1800
	s_waitcnt lgkmcnt(1)
	s_nop 0
	v_mfma_f32_16x16x32_bf16 v[82:85], v[196:199], v[246:249], v[82:85]
	v_mfma_f32_16x16x32_bf16 v[92:95], v[222:225], v[246:249], v[92:95]
	v_mfma_f32_16x16x32_bf16 v[96:99], v[226:229], v[246:249], v[96:99]
	v_mfma_f32_16x16x32_bf16 v[104:107], v[238:241], v[246:249], v[104:107]
	ds_read_b128 v[246:249], v216 offset:0x1c00
	s_waitcnt lgkmcnt(1)
	s_nop 0
	v_mfma_f32_16x16x32_bf16 v[116:119], v[196:199], v[242:245], v[116:119]
	v_mfma_f32_16x16x32_bf16 v[124:127], v[222:225], v[242:245], v[124:127]
	v_mfma_f32_16x16x32_bf16 v[132:135], v[226:229], v[242:245], v[132:135]
	v_mfma_f32_16x16x32_bf16 v[136:139], v[238:241], v[242:245], v[136:139]
	ds_read_b128 v[242:245], v216 offset:0x2000
	s_waitcnt lgkmcnt(1)
	s_nop 0
	v_mfma_f32_16x16x32_bf16 v[120:123], v[196:199], v[246:249], v[120:123]
	v_mfma_f32_16x16x32_bf16 v[128:131], v[222:225], v[246:249], v[128:131]
	v_mfma_f32_16x16x32_bf16 v[140:143], v[226:229], v[246:249], v[140:143]
	v_mfma_f32_16x16x32_bf16 v[144:147], v[238:241], v[246:249], v[144:147]
	ds_read_b128 v[246:249], v216 offset:0x2400
	s_waitcnt lgkmcnt(1)
	s_nop 0
	v_mfma_f32_16x16x32_bf16 v[148:151], v[196:199], v[242:245], v[148:151]
	s_waitcnt lgkmcnt(0)
	v_mfma_f32_16x16x32_bf16 v[176:179], v[222:225], v[242:245], v[176:179]
	v_mfma_f32_16x16x32_bf16 v[172:175], v[226:229], v[242:245], v[172:175]
	v_mfma_f32_16x16x32_bf16 v[168:171], v[238:241], v[242:245], v[168:171]
	v_mfma_f32_16x16x32_bf16 v[164:167], v[196:199], v[246:249], v[164:167]
	v_mfma_f32_16x16x32_bf16 v[160:163], v[222:225], v[246:249], v[160:163]
	v_mfma_f32_16x16x32_bf16 v[156:159], v[226:229], v[246:249], v[156:159]
	v_mfma_f32_16x16x32_bf16 v[152:155], v[238:241], v[246:249], v[152:155]
	s_cmp_lt_u32 s5, 14
	s_cbranch_scc0 .Lstg_b57916
	s_cmp_eq_u32 s55, 0
	s_cbranch_scc1 .Lstg_b57916
	v_lshl_add_u64 v[180:181], v[200:201], 0, s[64:65]
	s_mov_b32 m0, s8
	s_nop 0
	global_load_lds_dwordx4 v[180:181], off
	v_lshl_add_u64 v[180:181], v[202:203], 0, s[64:65]
	s_add_i32 m0, s8, 0x400
	s_nop 0
	global_load_lds_dwordx4 v[180:181], off
	v_lshl_add_u64 v[180:181], v[204:205], 0, s[64:65]
	s_add_i32 m0, s8, 0x800
	s_nop 0
	global_load_lds_dwordx4 v[180:181], off
	v_lshl_add_u64 v[180:181], v[206:207], 0, s[64:65]
	s_add_i32 m0, s8, 0xc00
	s_nop 0
	global_load_lds_dwordx4 v[180:181], off
	v_lshl_add_u64 v[180:181], v[208:209], 0, s[64:65]
	s_lshl_b32 s64, s6, 18
	s_add_i32 m0, s8, 0x1000
	v_lshl_add_u64 v[184:185], v[210:211], 0, s[64:65]
	global_load_lds_dwordx4 v[180:181], off
	global_load_dwordx4 v[180:183], v[184:185], off nt
	v_add_co_u32_e32 v184, vcc, s33, v184
	s_nop 1
	v_addc_co_u32_e32 v185, vcc, 0, v185, vcc
	global_load_dwordx4 v[184:187], v[184:185], off nt
